# stack4: stack3 + expert stage 1 reads the activation fragments of each k-step from LDS one k-step ahead (two register sets)
# baseline (speedup 1.0000x reference)
; #define LD32(p_) CAT8(*(const i32x4v*)(p_), *(const i32x4v*)((p_) + 16))
; #define AFRAG(mi_, ks_) CAT8(*(const i32x4v*)(smem + aoff + (mi_) * 16384 + (((8 * (ks_) + 2 * g) ^ lr) << 4)), *(const i32x4v*)(smem + aoff + (mi_) * 16384 + (((8 * (ks_) + 2 * g + 1) ^ lr) << 4)))
; #define AFRAG(hb_, mi_, ks_) CAT8(*(const i32x4v*)((hb_) + aoff + (mi_) * 4096 + (((8 * (ks_) + 2 * g2) ^ lr2) << 4)), *(const i32x4v*)((hb_) + aoff + (mi_) * 4096 + (((8 * (ks_) + 2 * g2 + 1) ^ lr2) << 4)))
; DEVINL void phase5(const Params& P, unsigned char* smem) {
;     ...
;         i32x8 b0[4];
; #pragma unroll
;         for (int j_ = 0; j_ < 4; ++j_) b0[j_] = LD32(P.ws + WS_WGUF + (size_t)e_lo * (8 * 32 * 2048) + (size_t)(4 * wv) * 2048 + j_ * 2048 + voff);
; #pragma unroll 1
;         for (int sx = 0; sx < 2; ++sx) {
;             const int e = sx ? e_hi : e_lo;
;             f32x4 acc[4][5];
; #pragma unroll
;             for (int i = 0; i < 4; ++i)
; #pragma unroll
;                 for (int mi = 0; mi < 5; ++mi) acc[i][mi] = (f32x4){0.f, 0.f, 0.f, 0.f};
;             const unsigned char* wb1 = P.ws + WS_WGUF + (size_t)e * (8 * 32 * 2048) + (size_t)(4 * wv) * 2048;
;             const int aoff = lr * 1024;
;     ...
;             const unsigned char* nxt_ = sx ? P.ws + WS_WDF + (size_t)e_lo * (2 * 64 * 2048) + (size_t)(8 * wv) * 2048 : P.ws + WS_WGUF + (size_t)e_hi * (8 * 32 * 2048) + (size_t)(4 * wv) * 2048;
; #pragma unroll 1
;             for (int ks = 0; ks < 8; ++ks) {
;                 i32x8 fa[5];
; #pragma unroll
;                 for (int mi_ = 0; mi_ < 5; ++mi_) fa[mi_] = AFRAG(mi_, ks);
.LBB0_720:
	s_or_b64 exec, exec, s[28:29]
	s_lshl_b32 s0, s35, 3
	s_or_b32 s49, s50, s0
	s_xor_b32 s0, s50, 15
	s_mul_i32 s0, s0, s50
	s_add_i32 s34, s34, s49
	s_lshr_b32 s0, s0, 1
	s_sub_i32 s0, s34, s0
	s_add_i32 s0, s0, 1
	s_lshl_b32 s1, s49, 19
	s_add_u32 s28, s37, s1
	s_addc_u32 s29, s38, 0
	v_lshl_add_u64 v[26:27], s[28:29], 0, v[194:195]
	s_waitcnt lgkmcnt(0)
	s_barrier
	global_load_dwordx4 v[2:5], v194, s[28:29]
	global_load_dwordx4 v[6:9], v194, s[28:29] offset:16
	global_load_dwordx4 v[10:13], v194, s[28:29] offset:2048
	global_load_dwordx4 v[14:17], v194, s[28:29] offset:2064
	v_add_co_u32_e32 v36, vcc, s45, v26
	v_lshl_add_u64 v[28:29], v[26:27], 0, s[14:15]
	s_nop 0
	v_addc_co_u32_e32 v37, vcc, 0, v27, vcc
	global_load_dwordx4 v[18:21], v[36:37], off
	global_load_dwordx4 v[22:25], v[28:29], off offset:16
	v_lshl_add_u64 v[38:39], v[26:27], 0, s[16:17]
	global_load_dwordx4 v[26:29], v[36:37], off offset:2048
	global_load_dwordx4 v[30:33], v[38:39], off offset:16
	s_ashr_i32 s1, s0, 31
	s_lshl_b32 s30, s49, 18
	s_lshl_b64 s[28:29], s[0:1], 19
	s_add_u32 s1, s39, s30
	s_waitcnt vmcnt(22)
	v_and_b32_e32 v114, 15, v34
	s_addc_u32 s50, s40, 0
	v_lshl_add_u32 v115, v114, 10, 0
	v_lshrrev_b32_e32 v34, 3, v34
	s_add_u32 s51, s37, s28
	s_mov_b32 s53, 0
	v_and_b32_e32 v116, 6, v34
	v_add_u32_e32 v117, 0x10000, v115
	s_addc_u32 s52, s38, s29
	s_mov_b64 s[30:31], -1
	s_lshl_b32 s60, s49, 19
	s_add_u32 s60, s41, s60
	s_addc_u32 s61, s42, 0
	s_add_u32 s62, s60, 0x1000
	s_addc_u32 s63, s61, 0
	v_mov_b32_e32 v118, v116
	v_add_u32_e32 v242, 1, v118
	v_xor_b32_e32 v243, v118, v114
	v_xor_b32_e32 v242, v242, v114
	v_lshlrev_b32_e32 v243, 4, v243
	v_lshlrev_b32_e32 v242, 4, v242
	v_add_u32_e32 v244, v115, v243
	v_add_u32_e32 v245, v115, v242
	v_add_u32_e32 v243, v117, v243
	v_add_u32_e32 v242, v117, v242
	ds_read_b128 v[166:169], v244
	ds_read_b128 v[174:177], v244 offset:16384
	ds_read_b128 v[170:173], v245
	ds_read_b128 v[178:181], v245 offset:16384
	ds_read_b128 v[182:185], v244 offset:32768
	ds_read_b128 v[198:201], v244 offset:49152
	ds_read_b128 v[186:189], v245 offset:32768
	ds_read_b128 v[202:205], v245 offset:49152
	ds_read_b128 v[206:209], v243
	ds_read_b128 v[210:213], v242
.LBB0_721:
	s_xor_b64 s[28:29], s[30:31], -1
	s_and_b64 s[90:91], s[30:31], exec
	s_cselect_b32 s82, s51, s1
	s_cselect_b32 s83, s52, s50
	s_mov_b32 s86, 0x20000
	s_cselect_b32 s86, 0x10000, s86
	s_mov_b32 s81, 0
	v_mov_b32_e32 v38, 0
	v_mov_b32_e32 v118, v116
	v_mov_b32_e32 v39, v38
	v_mov_b32_e32 v40, v38
	v_mov_b32_e32 v41, v38
	v_mov_b32_e32 v50, v38
	v_mov_b32_e32 v51, v38
	v_mov_b32_e32 v52, v38
	v_mov_b32_e32 v53, v38
	v_mov_b32_e32 v58, v38
	v_mov_b32_e32 v59, v38
	v_mov_b32_e32 v60, v38
	v_mov_b32_e32 v61, v38
	v_mov_b32_e32 v66, v38
	v_mov_b32_e32 v67, v38
	v_mov_b32_e32 v68, v38
	v_mov_b32_e32 v69, v38
	v_mov_b32_e32 v34, v38
	v_mov_b32_e32 v35, v38
	v_mov_b32_e32 v36, v38
	v_mov_b32_e32 v37, v38
	v_mov_b32_e32 v46, v38
	v_mov_b32_e32 v47, v38
	v_mov_b32_e32 v48, v38
	v_mov_b32_e32 v49, v38
	v_mov_b32_e32 v54, v38
	v_mov_b32_e32 v55, v38
	v_mov_b32_e32 v56, v38
	v_mov_b32_e32 v57, v38
	v_mov_b32_e32 v62, v38
	v_mov_b32_e32 v63, v38
	v_mov_b32_e32 v64, v38
	v_mov_b32_e32 v65, v38
	v_mov_b32_e32 v70, v38
	v_mov_b32_e32 v71, v38
	v_mov_b32_e32 v72, v38
	v_mov_b32_e32 v73, v38
	v_mov_b32_e32 v74, v38
	v_mov_b32_e32 v75, v38
	v_mov_b32_e32 v76, v38
	v_mov_b32_e32 v77, v38
	v_mov_b32_e32 v82, v38
	v_mov_b32_e32 v83, v38
	v_mov_b32_e32 v84, v38
	v_mov_b32_e32 v85, v38
	v_mov_b32_e32 v90, v38
	v_mov_b32_e32 v91, v38
	v_mov_b32_e32 v92, v38
	v_mov_b32_e32 v93, v38
	v_mov_b32_e32 v98, v38
	v_mov_b32_e32 v99, v38
	v_mov_b32_e32 v100, v38
	v_mov_b32_e32 v101, v38
	v_mov_b32_e32 v106, v38
	v_mov_b32_e32 v107, v38
	v_mov_b32_e32 v108, v38
	v_mov_b32_e32 v109, v38
	v_mov_b32_e32 v78, v38
	v_mov_b32_e32 v79, v38
	v_mov_b32_e32 v80, v38
	v_mov_b32_e32 v81, v38
	v_mov_b32_e32 v86, v38
	v_mov_b32_e32 v87, v38
	v_mov_b32_e32 v88, v38
	v_mov_b32_e32 v89, v38
	v_mov_b32_e32 v94, v38
	v_mov_b32_e32 v95, v38
	v_mov_b32_e32 v96, v38
	v_mov_b32_e32 v97, v38
	v_mov_b32_e32 v102, v38
	v_mov_b32_e32 v103, v38
	v_mov_b32_e32 v104, v38
	v_mov_b32_e32 v105, v38
	v_mov_b32_e32 v110, v38
	v_mov_b32_e32 v111, v38
	v_mov_b32_e32 v112, v38
	v_mov_b32_e32 v113, v38
	v_mov_b32_e32 v42, v38
	v_mov_b32_e32 v43, v38
	v_mov_b32_e32 v44, v38
	v_mov_b32_e32 v45, v38
; #define MX(a_, b_, c_) __builtin_amdgcn_mfma_scale_f32_16x16x128_f8f6f4(a_, b_, c_, 0, 0, 0, 0x7f7f7f7f, 0, 0x7f7f7f7f)
; #define LD32(p_) CAT8(*(const i32x4v*)(p_), *(const i32x4v*)((p_) + 16))
; #define AFRAG(mi_, ks_) CAT8(*(const i32x4v*)(smem + aoff + (mi_) * 16384 + (((8 * (ks_) + 2 * g) ^ lr) << 4)), *(const i32x4v*)(smem + aoff + (mi_) * 16384 + (((8 * (ks_) + 2 * g + 1) ^ lr) << 4)))
; #define AFRAG(hb_, mi_, ks_) CAT8(*(const i32x4v*)((hb_) + aoff + (mi_) * 4096 + (((8 * (ks_) + 2 * g2) ^ lr2) << 4)), *(const i32x4v*)((hb_) + aoff + (mi_) * 4096 + (((8 * (ks_) + 2 * g2 + 1) ^ lr2) << 4)))
; DEVINL void phase5(const Params& P, unsigned char* smem) {
;     ...
; #pragma unroll 1
;             for (int ks = 0; ks < 8; ++ks) {
;                 i32x8 fa[5];
; #pragma unroll
;                 for (int mi_ = 0; mi_ < 5; ++mi_) fa[mi_] = AFRAG(mi_, ks);
;                 const unsigned char* un_ = ks + 1 < 8 ? wb1 + (size_t)((ks + 1) * 32) * 2048 : nxt_;
; #pragma unroll
;                 for (int j_ = 0; j_ < 4; ++j_) {
; #pragma unroll
;                     for (int mi_ = 0; mi_ < 5; ++mi_) acc[j_][mi_] = MX(b0[j_], fa[mi_], acc[j_][mi_]);
;                     b0[j_] = LD32(un_ + j_ * 2048 + voff);
;                     __builtin_amdgcn_sched_barrier(0);
;                 }
;             }
.LBB0_722:
	s_waitcnt lgkmcnt(0)
	v_add_u32_e32 v118, 8, v118
	v_add_u32_e32 v120, 1, v118
	v_xor_b32_e32 v119, v118, v114
	v_xor_b32_e32 v120, v120, v114
	v_lshlrev_b32_e32 v119, 4, v119
	v_lshlrev_b32_e32 v152, 4, v120
	v_add_u32_e32 v140, v115, v119
	v_add_u32_e32 v148, v115, v152
	v_add_u32_e32 v119, v117, v119
	v_add_u32_e32 v156, v117, v152
	ds_read_b128 v[120:123], v140
	ds_read_b128 v[128:131], v140 offset:16384
	ds_read_b128 v[124:127], v148
	ds_read_b128 v[132:135], v148 offset:16384
	ds_read_b128 v[136:139], v140 offset:32768
	ds_read_b128 v[144:147], v140 offset:49152
	ds_read_b128 v[140:143], v148 offset:32768
	ds_read_b128 v[148:151], v148 offset:49152
	ds_read_b128 v[152:155], v119
	ds_read_b128 v[156:159], v156
	s_waitcnt vmcnt(6)
	v_mfma_scale_f32_16x16x128_f8f6f4 v[110:113], v[2:9], v[166:173], v[110:113], v220, v220 op_sel_hi:[0,0,0]
	v_mfma_scale_f32_16x16x128_f8f6f4 v[102:105], v[2:9], v[174:181], v[102:105], v220, v220 op_sel_hi:[0,0,0]
	v_mfma_scale_f32_16x16x128_f8f6f4 v[94:97], v[2:9], v[182:189], v[94:97], v220, v220 op_sel_hi:[0,0,0]
	v_mfma_scale_f32_16x16x128_f8f6f4 v[86:89], v[2:9], v[198:205], v[86:89], v220, v220 op_sel_hi:[0,0,0]
	v_mfma_scale_f32_16x16x128_f8f6f4 v[78:81], v[2:9], v[206:213], v[78:81], v220, v220 op_sel_hi:[0,0,0]
	global_load_dwordx4 v[2:5], v194, s[60:61]
	global_load_dwordx4 v[6:9], v194, s[60:61] offset:16
	s_waitcnt vmcnt(6)
	v_mfma_scale_f32_16x16x128_f8f6f4 v[106:109], v[10:17], v[166:173], v[106:109], v220, v220 op_sel_hi:[0,0,0]
	v_mfma_scale_f32_16x16x128_f8f6f4 v[98:101], v[10:17], v[174:181], v[98:101], v220, v220 op_sel_hi:[0,0,0]
	v_mfma_scale_f32_16x16x128_f8f6f4 v[90:93], v[10:17], v[182:189], v[90:93], v220, v220 op_sel_hi:[0,0,0]
	v_mfma_scale_f32_16x16x128_f8f6f4 v[82:85], v[10:17], v[198:205], v[82:85], v220, v220 op_sel_hi:[0,0,0]
	v_mfma_scale_f32_16x16x128_f8f6f4 v[74:77], v[10:17], v[206:213], v[74:77], v220, v220 op_sel_hi:[0,0,0]
	global_load_dwordx4 v[10:13], v194, s[60:61] offset:2048
	global_load_dwordx4 v[14:17], v194, s[60:61] offset:2064
	s_waitcnt vmcnt(6)
	v_mfma_scale_f32_16x16x128_f8f6f4 v[70:73], v[18:25], v[166:173], v[70:73], v220, v220 op_sel_hi:[0,0,0]
	v_mfma_scale_f32_16x16x128_f8f6f4 v[62:65], v[18:25], v[174:181], v[62:65], v220, v220 op_sel_hi:[0,0,0]
	v_mfma_scale_f32_16x16x128_f8f6f4 v[54:57], v[18:25], v[182:189], v[54:57], v220, v220 op_sel_hi:[0,0,0]
	v_mfma_scale_f32_16x16x128_f8f6f4 v[46:49], v[18:25], v[198:205], v[46:49], v220, v220 op_sel_hi:[0,0,0]
	v_mfma_scale_f32_16x16x128_f8f6f4 v[34:37], v[18:25], v[206:213], v[34:37], v220, v220 op_sel_hi:[0,0,0]
	global_load_dwordx4 v[18:21], v194, s[62:63]
	global_load_dwordx4 v[22:25], v194, s[62:63] offset:16
	s_waitcnt vmcnt(6)
	v_mfma_scale_f32_16x16x128_f8f6f4 v[66:69], v[26:33], v[166:173], v[66:69], v220, v220 op_sel_hi:[0,0,0]
	v_mfma_scale_f32_16x16x128_f8f6f4 v[58:61], v[26:33], v[174:181], v[58:61], v220, v220 op_sel_hi:[0,0,0]
	v_mfma_scale_f32_16x16x128_f8f6f4 v[50:53], v[26:33], v[182:189], v[50:53], v220, v220 op_sel_hi:[0,0,0]
	v_mfma_scale_f32_16x16x128_f8f6f4 v[38:41], v[26:33], v[198:205], v[38:41], v220, v220 op_sel_hi:[0,0,0]
	v_mfma_scale_f32_16x16x128_f8f6f4 v[42:45], v[26:33], v[206:213], v[42:45], v220, v220 op_sel_hi:[0,0,0]
	global_load_dwordx4 v[26:29], v194, s[62:63] offset:2048
	global_load_dwordx4 v[30:33], v194, s[62:63] offset:2064
	s_add_u32 s60, s60, 0x10000
	s_addc_u32 s61, s61, 0
	s_cmp_eq_u32 s81, 3
	s_cselect_b32 s60, s82, s60
	s_cselect_b32 s61, s83, s61
	s_add_u32 s62, s60, 0x1000
	s_addc_u32 s63, s61, 0
	s_waitcnt lgkmcnt(0)
	v_add_u32_e32 v118, 8, v118
	v_and_b32_e32 v118, 63, v118
	v_add_u32_e32 v242, 1, v118
	v_xor_b32_e32 v243, v118, v114
	v_xor_b32_e32 v242, v242, v114
	v_lshlrev_b32_e32 v243, 4, v243
	v_lshlrev_b32_e32 v242, 4, v242
	v_add_u32_e32 v244, v115, v243
	v_add_u32_e32 v245, v115, v242
	v_add_u32_e32 v243, v117, v243
	v_add_u32_e32 v242, v117, v242
	ds_read_b128 v[166:169], v244
	ds_read_b128 v[174:177], v244 offset:16384
	ds_read_b128 v[170:173], v245
	ds_read_b128 v[178:181], v245 offset:16384
	ds_read_b128 v[182:185], v244 offset:32768
	ds_read_b128 v[198:201], v244 offset:49152
	ds_read_b128 v[186:189], v245 offset:32768
	ds_read_b128 v[202:205], v245 offset:49152
	ds_read_b128 v[206:209], v243
	ds_read_b128 v[210:213], v242
	s_waitcnt vmcnt(6)
	v_mfma_scale_f32_16x16x128_f8f6f4 v[110:113], v[2:9], v[120:127], v[110:113], v220, v220 op_sel_hi:[0,0,0]
	v_mfma_scale_f32_16x16x128_f8f6f4 v[102:105], v[2:9], v[128:135], v[102:105], v220, v220 op_sel_hi:[0,0,0]
	v_mfma_scale_f32_16x16x128_f8f6f4 v[94:97], v[2:9], v[136:143], v[94:97], v220, v220 op_sel_hi:[0,0,0]
	v_mfma_scale_f32_16x16x128_f8f6f4 v[86:89], v[2:9], v[144:151], v[86:89], v220, v220 op_sel_hi:[0,0,0]
	v_mfma_scale_f32_16x16x128_f8f6f4 v[78:81], v[2:9], v[152:159], v[78:81], v220, v220 op_sel_hi:[0,0,0]
	global_load_dwordx4 v[2:5], v194, s[60:61]
	global_load_dwordx4 v[6:9], v194, s[60:61] offset:16
	s_waitcnt vmcnt(6)
	v_mfma_scale_f32_16x16x128_f8f6f4 v[106:109], v[10:17], v[120:127], v[106:109], v220, v220 op_sel_hi:[0,0,0]
	v_mfma_scale_f32_16x16x128_f8f6f4 v[98:101], v[10:17], v[128:135], v[98:101], v220, v220 op_sel_hi:[0,0,0]
	v_mfma_scale_f32_16x16x128_f8f6f4 v[90:93], v[10:17], v[136:143], v[90:93], v220, v220 op_sel_hi:[0,0,0]
	v_mfma_scale_f32_16x16x128_f8f6f4 v[82:85], v[10:17], v[144:151], v[82:85], v220, v220 op_sel_hi:[0,0,0]
	v_mfma_scale_f32_16x16x128_f8f6f4 v[74:77], v[10:17], v[152:159], v[74:77], v220, v220 op_sel_hi:[0,0,0]
	global_load_dwordx4 v[10:13], v194, s[60:61] offset:2048
	global_load_dwordx4 v[14:17], v194, s[60:61] offset:2064
	s_waitcnt vmcnt(6)
; DEVINL float sat8(float v) { return __builtin_amdgcn_fmed3f(v, -448.f, 448.f); }
; #define MX(a_, b_, c_) __builtin_amdgcn_mfma_scale_f32_16x16x128_f8f6f4(a_, b_, c_, 0, 0, 0, 0x7f7f7f7f, 0, 0x7f7f7f7f)
; #define LD32(p_) CAT8(*(const i32x4v*)(p_), *(const i32x4v*)((p_) + 16))
; DEVINL void phase5(const Params& P, unsigned char* smem) {
;     ...
;                 const unsigned char* un_ = ks + 1 < 8 ? wb1 + (size_t)((ks + 1) * 32) * 2048 : nxt_;
; #pragma unroll
;                 for (int j_ = 0; j_ < 4; ++j_) {
; #pragma unroll
;                     for (int mi_ = 0; mi_ < 5; ++mi_) acc[j_][mi_] = MX(b0[j_], fa[mi_], acc[j_][mi_]);
;                     b0[j_] = LD32(un_ + j_ * 2048 + voff);
;                     __builtin_amdgcn_sched_barrier(0);
;                 }
;             }
;     ...
;             int l1 = lane;
;             asm volatile("" : "+v"(l1));
;             const int lrh = l1 & 15, gh = l1 >> 4;
;             unsigned char* hsm = hs0 + sx * 20480;
;             const float* swt = sx ? s_wh : s_wl;
; #pragma unroll
;             for (int p = 0; p < 2; ++p)
; #pragma unroll
;                 for (int mi = 0; mi < 5; ++mi) {
;                     const int row = 16 * mi + lrh, c16 = 2 * wv + p;
;                     const float ws_ = swt[row] * (8.f / 32.f);
;                     const f32x4 gt = acc[2 * p][mi] * (1.f / 32.f), up = acc[2 * p + 1][mi] * ws_;
;                     const unsigned o = pk4_fp8(sat8(gt.x * __builtin_amdgcn_rcpf(1.f + __expf(-gt.x)) * up.x), sat8(gt.y * __builtin_amdgcn_rcpf(1.f + __expf(-gt.y)) * up.y), sat8(gt.z * __builtin_amdgcn_rcpf(1.f + __expf(-gt.z)) * up.z), sat8(gt.w * __builtin_amdgcn_rcpf(1.f + __expf(-gt.w)) * up.w));
	v_mfma_scale_f32_16x16x128_f8f6f4 v[70:73], v[18:25], v[120:127], v[70:73], v220, v220 op_sel_hi:[0,0,0]
	v_mfma_scale_f32_16x16x128_f8f6f4 v[62:65], v[18:25], v[128:135], v[62:65], v220, v220 op_sel_hi:[0,0,0]
	v_mfma_scale_f32_16x16x128_f8f6f4 v[54:57], v[18:25], v[136:143], v[54:57], v220, v220 op_sel_hi:[0,0,0]
	v_mfma_scale_f32_16x16x128_f8f6f4 v[46:49], v[18:25], v[144:151], v[46:49], v220, v220 op_sel_hi:[0,0,0]
	v_mfma_scale_f32_16x16x128_f8f6f4 v[34:37], v[18:25], v[152:159], v[34:37], v220, v220 op_sel_hi:[0,0,0]
	global_load_dwordx4 v[18:21], v194, s[62:63]
	global_load_dwordx4 v[22:25], v194, s[62:63] offset:16
	s_waitcnt vmcnt(6)
	v_mfma_scale_f32_16x16x128_f8f6f4 v[66:69], v[26:33], v[120:127], v[66:69], v220, v220 op_sel_hi:[0,0,0]
	v_mfma_scale_f32_16x16x128_f8f6f4 v[58:61], v[26:33], v[128:135], v[58:61], v220, v220 op_sel_hi:[0,0,0]
	v_mfma_scale_f32_16x16x128_f8f6f4 v[50:53], v[26:33], v[136:143], v[50:53], v220, v220 op_sel_hi:[0,0,0]
	v_mfma_scale_f32_16x16x128_f8f6f4 v[38:41], v[26:33], v[144:151], v[38:41], v220, v220 op_sel_hi:[0,0,0]
	v_mfma_scale_f32_16x16x128_f8f6f4 v[42:45], v[26:33], v[152:159], v[42:45], v220, v220 op_sel_hi:[0,0,0]
	global_load_dwordx4 v[26:29], v194, s[62:63] offset:2048
	global_load_dwordx4 v[30:33], v194, s[62:63] offset:2064
	s_cmp_eq_u32 s81, 3
	s_cselect_b32 s90, s86, 0x10000
	s_add_u32 s60, s60, s90
	s_addc_u32 s61, s61, 0
	s_add_u32 s62, s60, 0x1000
	s_addc_u32 s63, s61, 0
	s_add_i32 s81, s81, 1
	s_cmp_eq_u32 s81, 4
	s_cbranch_scc0 .LBB0_722
	s_add_i32 s34, s53, 0
	s_add_i32 s34, s34, 0x14000
	s_and_b64 s[30:31], s[30:31], exec
	v_mov_b32_e32 v122, v223
	s_cselect_b32 s30, 0x24a40, s44
	s_add_i32 s30, s30, 0
	v_and_b32_e32 v123, 15, v122
	v_ashrrev_i32_e32 v118, 2, v122
	v_and_b32_e32 v118, -4, v118
	v_lshl_add_u32 v125, v123, 2, s30
	v_add_u32_e32 v124, s34, v118
	ds_read2_b32 v[118:119], v125 offset1:16
	v_pk_mul_f32 v[120:121], v[110:111], s[18:19] op_sel_hi:[1,0]
	v_pk_mul_f32 v[112:113], v[112:113], s[18:19] op_sel_hi:[1,0]
	v_mul_f32_e32 v110, 0xbfb8aa3b, v120
	v_exp_f32_e32 v111, v110
	s_waitcnt lgkmcnt(0)
	v_mul_f32_e32 v110, 0x3e800000, v118
	v_mul_f32_e32 v118, 0xbfb8aa3b, v121
	v_exp_f32_e32 v118, v118
	v_pk_mul_f32 v[108:109], v[108:109], v[110:111] op_sel_hi:[1,0]
	v_add_f32_e32 v111, 1.0, v111
	v_rcp_f32_e32 v111, v111
	v_bitop3_b32 v126, v122, s19, 15 bitop3:0x6c
	v_pk_mul_f32 v[104:105], v[104:105], s[18:19] op_sel_hi:[1,0]
	v_pk_mul_f32 v[96:97], v[96:97], s[18:19] op_sel_hi:[1,0]
	v_pk_mul_f32 v[106:107], v[106:107], v[110:111] op_sel_hi:[1,0]
	v_mul_f32_e32 v111, v120, v111
	v_mul_f32_e32 v106, v111, v106
	v_add_f32_e32 v111, 1.0, v118
	v_rcp_f32_e32 v111, v111
	v_mul_f32_e32 v118, 0xbfb8aa3b, v112
	v_exp_f32_e32 v118, v118
	v_med3_f32 v106, v106, s46, v222
	v_mul_f32_e32 v111, v121, v111
	v_mul_f32_e32 v107, v111, v107
	v_add_f32_e32 v111, 1.0, v118
	v_rcp_f32_e32 v111, v111
	v_mul_f32_e32 v118, 0xbfb8aa3b, v113
	v_exp_f32_e32 v118, v118
	v_med3_f32 v107, v107, s46, v222
	v_mul_f32_e32 v111, v112, v111
	v_mul_f32_e32 v108, v111, v108
	v_add_f32_e32 v111, 1.0, v118
	v_rcp_f32_e32 v111, v111
	v_mov_b32_e32 v112, 0
	v_cvt_pk_fp8_f32 v112, v106, v107
	v_med3_f32 v108, v108, s46, v222
	v_mul_f32_e32 v106, v113, v111
	v_mul_f32_e32 v106, v106, v109
	v_med3_f32 v106, v106, s46, v222
	v_cvt_pk_fp8_f32 v112, v108, v106 op_sel:[0,0,1]
	v_lshl_add_u32 v108, v126, 4, v124
	v_lshlrev_b32_e32 v109, 8, v123
	v_add_u32_e32 v106, v108, v109
	ds_write_b32 v106, v112
	v_pk_mul_f32 v[106:107], v[102:103], s[18:19] op_sel_hi:[1,0]
	v_pk_mul_f32 v[88:89], v[88:89], s[18:19] op_sel_hi:[1,0]
	v_mul_f32_e32 v102, 0xbfb8aa3b, v106
	v_exp_f32_e32 v103, v102
	v_mul_f32_e32 v102, 0x3e800000, v119
	v_mul_f32_e32 v111, 0xbfb8aa3b, v107
	v_exp_f32_e32 v111, v111
	v_pk_mul_f32 v[100:101], v[100:101], v[102:103] op_sel_hi:[1,0]
	v_add_f32_e32 v103, 1.0, v103
	v_rcp_f32_e32 v103, v103
	v_pk_mul_f32 v[80:81], v[80:81], s[18:19] op_sel_hi:[1,0]
	v_pk_mul_f32 v[70:71], v[70:71], s[18:19] op_sel_hi:[1,0]
	v_pk_mul_f32 v[66:67], v[66:67], v[110:111] op_sel_hi:[1,0]
	v_pk_mul_f32 v[98:99], v[98:99], v[102:103] op_sel_hi:[1,0]
	v_mul_f32_e32 v103, v106, v103
	v_mul_f32_e32 v98, v103, v98
	v_add_f32_e32 v103, 1.0, v111
	v_rcp_f32_e32 v103, v103
	v_mul_f32_e32 v106, 0xbfb8aa3b, v104
	v_exp_f32_e32 v106, v106
	v_med3_f32 v98, v98, s46, v222
	v_mul_f32_e32 v103, v107, v103
	v_mul_f32_e32 v99, v103, v99
	v_add_f32_e32 v103, 1.0, v106
	v_rcp_f32_e32 v103, v103
	v_mul_f32_e32 v106, 0xbfb8aa3b, v105
	v_exp_f32_e32 v106, v106
	v_med3_f32 v99, v99, s46, v222
	v_mul_f32_e32 v103, v104, v103
	v_mul_f32_e32 v100, v103, v100
	v_add_f32_e32 v103, 1.0, v106
	v_rcp_f32_e32 v103, v103
	v_mov_b32_e32 v104, 0
	v_cvt_pk_fp8_f32 v104, v98, v99
	v_med3_f32 v100, v100, s46, v222
	v_mul_f32_e32 v98, v105, v103
	v_mul_f32_e32 v98, v98, v101
	v_med3_f32 v98, v98, s46, v222
	v_cvt_pk_fp8_f32 v104, v100, v98 op_sel:[0,0,1]
	ds_read2_b32 v[98:99], v125 offset0:32 offset1:48
	v_pk_mul_f32 v[100:101], v[94:95], s[18:19] op_sel_hi:[1,0]
	v_pk_mul_f32 v[72:73], v[72:73], s[18:19] op_sel_hi:[1,0]
	v_mul_f32_e32 v94, 0xbfb8aa3b, v100
	v_exp_f32_e32 v95, v94
	s_waitcnt lgkmcnt(0)
; DEVINL float sat8(float v) { return __builtin_amdgcn_fmed3f(v, -448.f, 448.f); }
; DEVINL void phase5(const Params& P, unsigned char* smem) {
;     ...
; #pragma unroll
;             for (int p = 0; p < 2; ++p)
; #pragma unroll
;                 for (int mi = 0; mi < 5; ++mi) {
;                     const int row = 16 * mi + lrh, c16 = 2 * wv + p;
;                     const float ws_ = swt[row] * (8.f / 32.f);
;                     const f32x4 gt = acc[2 * p][mi] * (1.f / 32.f), up = acc[2 * p + 1][mi] * ws_;
;                     const unsigned o = pk4_fp8(sat8(gt.x * __builtin_amdgcn_rcpf(1.f + __expf(-gt.x)) * up.x), sat8(gt.y * __builtin_amdgcn_rcpf(1.f + __expf(-gt.y)) * up.y), sat8(gt.z * __builtin_amdgcn_rcpf(1.f + __expf(-gt.z)) * up.z), sat8(gt.w * __builtin_amdgcn_rcpf(1.f + __expf(-gt.w)) * up.w));
;                     *(unsigned*)(hsm + row * 256 + ((c16 ^ (row & 15)) << 4) + 4 * gh) = o;
;                 }
	v_mul_f32_e32 v94, 0x3e800000, v98
	v_mul_f32_e32 v98, 0xbfb8aa3b, v101
	v_exp_f32_e32 v98, v98
	v_pk_mul_f32 v[92:93], v[92:93], v[94:95] op_sel_hi:[1,0]
	v_add_f32_e32 v95, 1.0, v95
	v_rcp_f32_e32 v95, v95
	v_pk_mul_f32 v[68:69], v[68:69], v[110:111] op_sel_hi:[1,0]
	v_or_b32_e32 v103, 0x1000, v109
	v_add_u32_e32 v105, v108, v103
	v_pk_mul_f32 v[90:91], v[90:91], v[94:95] op_sel_hi:[1,0]
	v_mul_f32_e32 v95, v100, v95
	v_mul_f32_e32 v90, v95, v90
	v_add_f32_e32 v95, 1.0, v98
	v_rcp_f32_e32 v95, v95
	v_mul_f32_e32 v98, 0xbfb8aa3b, v96
	v_exp_f32_e32 v98, v98
	v_med3_f32 v90, v90, s46, v222
	v_mul_f32_e32 v95, v101, v95
	v_mul_f32_e32 v91, v95, v91
	v_add_f32_e32 v95, 1.0, v98
	v_rcp_f32_e32 v95, v95
	v_mul_f32_e32 v98, 0xbfb8aa3b, v97
	v_exp_f32_e32 v98, v98
	v_med3_f32 v91, v91, s46, v222
	v_mul_f32_e32 v95, v96, v95
	v_mul_f32_e32 v92, v95, v92
	v_add_f32_e32 v95, 1.0, v98
	v_rcp_f32_e32 v95, v95
	v_mov_b32_e32 v96, 0
	v_cvt_pk_fp8_f32 v96, v90, v91
	v_med3_f32 v92, v92, s46, v222
	v_mul_f32_e32 v90, v97, v95
	v_mul_f32_e32 v90, v90, v93
	v_med3_f32 v90, v90, s46, v222
	v_cvt_pk_fp8_f32 v96, v92, v90 op_sel:[0,0,1]
	v_or_b32_e32 v92, 0x2000, v109
	v_add_u32_e32 v90, v108, v92
	v_pk_mul_f32 v[62:63], v[62:63], s[18:19] op_sel_hi:[1,0]
	ds_write_b32 v90, v96
	v_pk_mul_f32 v[90:91], v[86:87], s[18:19] op_sel_hi:[1,0]
	ds_write_b32 v105, v104
	v_mul_f32_e32 v86, 0xbfb8aa3b, v90
	v_exp_f32_e32 v87, v86
	v_mul_f32_e32 v86, 0x3e800000, v99
	v_mul_f32_e32 v93, 0xbfb8aa3b, v91
	v_exp_f32_e32 v93, v93
	v_pk_mul_f32 v[84:85], v[84:85], v[86:87] op_sel_hi:[1,0]
	v_add_f32_e32 v87, 1.0, v87
	v_rcp_f32_e32 v87, v87
	v_pk_mul_f32 v[58:59], v[58:59], v[102:103] op_sel_hi:[1,0]
	v_pk_mul_f32 v[64:65], v[64:65], s[18:19] op_sel_hi:[1,0]
	v_pk_mul_f32 v[60:61], v[60:61], v[102:103] op_sel_hi:[1,0]
	v_pk_mul_f32 v[82:83], v[82:83], v[86:87] op_sel_hi:[1,0]
	v_mul_f32_e32 v87, v90, v87
	v_mul_f32_e32 v82, v87, v82
	v_add_f32_e32 v87, 1.0, v93
	v_rcp_f32_e32 v87, v87
	v_mul_f32_e32 v90, 0xbfb8aa3b, v88
	v_exp_f32_e32 v90, v90
	v_med3_f32 v82, v82, s46, v222
	v_mul_f32_e32 v87, v91, v87
	v_mul_f32_e32 v83, v87, v83
	v_add_f32_e32 v87, 1.0, v90
	v_rcp_f32_e32 v87, v87
	v_mul_f32_e32 v90, 0xbfb8aa3b, v89
	v_exp_f32_e32 v90, v90
	v_med3_f32 v83, v83, s46, v222
	v_mul_f32_e32 v87, v88, v87
	v_mul_f32_e32 v84, v87, v84
	v_add_f32_e32 v87, 1.0, v90
	v_rcp_f32_e32 v87, v87
	v_mov_b32_e32 v88, 0
	v_cvt_pk_fp8_f32 v88, v82, v83
	v_med3_f32 v84, v84, s46, v222
	v_mul_f32_e32 v82, v89, v87
	v_mul_f32_e32 v82, v82, v85
	v_med3_f32 v82, v82, s46, v222
	v_cvt_pk_fp8_f32 v88, v84, v82 op_sel:[0,0,1]
	v_or_b32_e32 v84, 0x3000, v109
	v_add_u32_e32 v82, v108, v84
	ds_read_b32 v85, v125 offset:256
	ds_write_b32 v82, v88
	v_pk_mul_f32 v[82:83], v[78:79], s[18:19] op_sel_hi:[1,0]
	v_pk_mul_f32 v[54:55], v[54:55], s[18:19] op_sel_hi:[1,0]
	v_mul_f32_e32 v78, 0xbfb8aa3b, v82
	v_exp_f32_e32 v79, v78
	s_waitcnt lgkmcnt(1)
	v_mul_f32_e32 v78, 0x3e800000, v85
	v_mul_f32_e32 v85, 0xbfb8aa3b, v83
	v_exp_f32_e32 v85, v85
	v_pk_mul_f32 v[76:77], v[76:77], v[78:79] op_sel_hi:[1,0]
	v_add_f32_e32 v79, 1.0, v79
	v_rcp_f32_e32 v79, v79
	v_pk_mul_f32 v[50:51], v[50:51], v[94:95] op_sel_hi:[1,0]
	v_pk_mul_f32 v[56:57], v[56:57], s[18:19] op_sel_hi:[1,0]
	v_pk_mul_f32 v[52:53], v[52:53], v[94:95] op_sel_hi:[1,0]
	v_pk_mul_f32 v[74:75], v[74:75], v[78:79] op_sel_hi:[1,0]
	v_mul_f32_e32 v79, v82, v79
	v_mul_f32_e32 v74, v79, v74
	v_add_f32_e32 v79, 1.0, v85
	v_rcp_f32_e32 v79, v79
	v_mul_f32_e32 v82, 0xbfb8aa3b, v80
	v_exp_f32_e32 v82, v82
	v_med3_f32 v74, v74, s46, v222
	v_mul_f32_e32 v79, v83, v79
	v_mul_f32_e32 v75, v79, v75
	v_add_f32_e32 v79, 1.0, v82
	v_rcp_f32_e32 v79, v79
	v_mul_f32_e32 v82, 0xbfb8aa3b, v81
	v_exp_f32_e32 v82, v82
	v_med3_f32 v75, v75, s46, v222
	v_mul_f32_e32 v79, v80, v79
	v_mul_f32_e32 v76, v79, v76
	v_add_f32_e32 v79, 1.0, v82
	v_rcp_f32_e32 v79, v79
	v_mov_b32_e32 v80, 0
	v_cvt_pk_fp8_f32 v80, v74, v75
	v_med3_f32 v76, v76, s46, v222
	v_mul_f32_e32 v74, v81, v79
	v_mul_f32_e32 v74, v74, v77
	v_med3_f32 v74, v74, s46, v222
	v_cvt_pk_fp8_f32 v80, v76, v74 op_sel:[0,0,1]
	v_mul_f32_e32 v76, 0xbfb8aa3b, v70
	v_exp_f32_e32 v76, v76
	v_or_b32_e32 v74, 0x4000, v109
	v_add_u32_e32 v75, v108, v74
	ds_write_b32 v75, v80
	v_add_f32_e32 v75, 1.0, v76
	v_rcp_f32_e32 v75, v75
	v_mul_f32_e32 v76, 0xbfb8aa3b, v71
	v_exp_f32_e32 v76, v76
	v_pk_mul_f32 v[46:47], v[46:47], s[18:19] op_sel_hi:[1,0]
	v_mul_f32_e32 v70, v70, v75
	v_mul_f32_e32 v66, v70, v66
	v_add_f32_e32 v70, 1.0, v76
	v_rcp_f32_e32 v70, v70
	v_mul_f32_e32 v75, 0xbfb8aa3b, v72
	v_exp_f32_e32 v75, v75
	v_med3_f32 v66, v66, s46, v222
	v_mul_f32_e32 v70, v71, v70
	v_mul_f32_e32 v67, v70, v67
	v_add_f32_e32 v70, 1.0, v75
	v_rcp_f32_e32 v70, v70
	v_mul_f32_e32 v71, 0xbfb8aa3b, v73
	v_exp_f32_e32 v71, v71
	v_med3_f32 v67, v67, s46, v222
	v_mul_f32_e32 v70, v72, v70
	v_mul_f32_e32 v68, v70, v68
	v_add_f32_e32 v70, 1.0, v71
	v_rcp_f32_e32 v70, v70
	v_mov_b32_e32 v71, 0
	v_cvt_pk_fp8_f32 v71, v66, v67
	v_med3_f32 v68, v68, s46, v222
	v_mul_f32_e32 v66, v73, v70
	v_mul_f32_e32 v66, v66, v69
	v_med3_f32 v66, v66, s46, v222
	v_cvt_pk_fp8_f32 v71, v68, v66 op_sel:[0,0,1]
	v_bitop3_b32 v66, v122, s36, 15 bitop3:0x6c
	v_lshl_add_u32 v66, v66, 4, v124
	v_add_u32_e32 v67, v66, v109
	ds_write_b32 v67, v71
	v_mul_f32_e32 v67, 0xbfb8aa3b, v62
	v_exp_f32_e32 v67, v67
	v_mul_f32_e32 v68, 0xbfb8aa3b, v63
	v_exp_f32_e32 v68, v68
	v_pk_mul_f32 v[38:39], v[38:39], v[86:87] op_sel_hi:[1,0]
	v_add_f32_e32 v67, 1.0, v67
	v_rcp_f32_e32 v67, v67
	v_add_f32_e32 v68, 1.0, v68
	v_rcp_f32_e32 v68, v68
	v_pk_mul_f32 v[48:49], v[48:49], s[18:19] op_sel_hi:[1,0]
; DEVINL float sat8(float v) { return __builtin_amdgcn_fmed3f(v, -448.f, 448.f); }
; DEVINL void phase5(const Params& P, unsigned char* smem) {
;     ...
; #pragma unroll
;             for (int p = 0; p < 2; ++p)
; #pragma unroll
;                 for (int mi = 0; mi < 5; ++mi) {
;                     const int row = 16 * mi + lrh, c16 = 2 * wv + p;
;                     const float ws_ = swt[row] * (8.f / 32.f);
;                     const f32x4 gt = acc[2 * p][mi] * (1.f / 32.f), up = acc[2 * p + 1][mi] * ws_;
;                     const unsigned o = pk4_fp8(sat8(gt.x * __builtin_amdgcn_rcpf(1.f + __expf(-gt.x)) * up.x), sat8(gt.y * __builtin_amdgcn_rcpf(1.f + __expf(-gt.y)) * up.y), sat8(gt.z * __builtin_amdgcn_rcpf(1.f + __expf(-gt.z)) * up.z), sat8(gt.w * __builtin_amdgcn_rcpf(1.f + __expf(-gt.w)) * up.w));
;                     *(unsigned*)(hsm + row * 256 + ((c16 ^ (row & 15)) << 4) + 4 * gh) = o;
;                 }
;         }
;         __syncthreads();
;         {
;             int l2 = lane;
;             asm volatile("" : "+v"(l2));
;             const int lr2 = l2 & 15, g2 = l2 >> 4;
;             const int aoff = lr2 * 256;
;             unsigned voff2 = (unsigned)(l2 * 32);
;     ...
;             u32x2 ypk[4][5];
;             f32x4 acc[4][5];
;             float q[5] = {0.f, 0.f, 0.f, 0.f, 0.f};
;             const unsigned char* wd0 = P.ws + WS_WDF + (size_t)(8 * wv) * 2048;
; #pragma unroll
;             for (int ph = 0; ph < 2; ++ph) {
; #pragma unroll
;                 for (int i = 0; i < 4; ++i)
; #pragma unroll
;                     for (int mi = 0; mi < 5; ++mi) acc[i][mi] = (f32x4){0.f, 0.f, 0.f, 0.f};
	v_mul_f32_e32 v62, v62, v67
	v_mul_f32_e32 v58, v62, v58
	v_mul_f32_e32 v62, v63, v68
	v_mul_f32_e32 v59, v62, v59
	v_mul_f32_e32 v62, 0xbfb8aa3b, v65
	v_exp_f32_e32 v62, v62
	v_med3_f32 v58, v58, s46, v222
	v_med3_f32 v59, v59, s46, v222
	v_mul_f32_e32 v63, 0xbfb8aa3b, v64
	v_add_f32_e32 v62, 1.0, v62
	v_rcp_f32_e32 v62, v62
	v_exp_f32_e32 v63, v63
	v_pk_mul_f32 v[40:41], v[40:41], v[86:87] op_sel_hi:[1,0]
	v_pk_mul_f32 v[34:35], v[34:35], s[18:19] op_sel_hi:[1,0]
	v_mul_f32_e32 v62, v65, v62
	v_mul_f32_e32 v61, v62, v61
	v_mov_b32_e32 v62, 0
	v_cvt_pk_fp8_f32 v62, v58, v59
	v_mul_f32_e32 v58, 0xbfb8aa3b, v54
	v_exp_f32_e32 v58, v58
	v_mul_f32_e32 v59, 0xbfb8aa3b, v55
	v_exp_f32_e32 v59, v59
	v_add_f32_e32 v63, 1.0, v63
	v_add_f32_e32 v58, 1.0, v58
	v_rcp_f32_e32 v58, v58
	v_rcp_f32_e32 v63, v63
	v_med3_f32 v61, v61, s46, v222
	v_pk_mul_f32 v[36:37], v[36:37], s[18:19] op_sel_hi:[1,0]
	v_mul_f32_e32 v54, v54, v58
	v_mul_f32_e32 v50, v54, v50
	v_add_f32_e32 v54, 1.0, v59
	v_rcp_f32_e32 v54, v54
	v_mul_f32_e32 v58, 0xbfb8aa3b, v56
	v_exp_f32_e32 v58, v58
	v_med3_f32 v50, v50, s46, v222
	v_mul_f32_e32 v54, v55, v54
	v_mul_f32_e32 v51, v54, v51
	v_add_f32_e32 v54, 1.0, v58
	v_rcp_f32_e32 v54, v54
	v_mul_f32_e32 v55, 0xbfb8aa3b, v57
	v_exp_f32_e32 v55, v55
	v_med3_f32 v51, v51, s46, v222
	v_mul_f32_e32 v54, v56, v54
	v_mul_f32_e32 v52, v54, v52
	v_add_f32_e32 v54, 1.0, v55
	v_rcp_f32_e32 v54, v54
	v_mov_b32_e32 v55, 0
	v_mul_f32_e32 v63, v64, v63
	v_cvt_pk_fp8_f32 v55, v50, v51
	v_mul_f32_e32 v60, v63, v60
	v_mul_f32_e32 v50, v57, v54
	v_med3_f32 v60, v60, s46, v222
	v_mul_f32_e32 v50, v50, v53
	v_cvt_pk_fp8_f32 v62, v60, v61 op_sel:[0,0,1]
	v_med3_f32 v52, v52, s46, v222
	v_med3_f32 v50, v50, s46, v222
	v_cvt_pk_fp8_f32 v55, v52, v50 op_sel:[0,0,1]
	v_add_u32_e32 v50, v66, v103
	ds_write_b32 v50, v62
	v_add_u32_e32 v50, v66, v92
	ds_write_b32 v50, v55
	v_mul_f32_e32 v50, 0xbfb8aa3b, v46
	v_exp_f32_e32 v50, v50
	v_mul_f32_e32 v51, 0xbfb8aa3b, v47
	v_exp_f32_e32 v51, v51
	s_movk_i32 s53, 0x5000
	v_add_f32_e32 v50, 1.0, v50
	v_rcp_f32_e32 v50, v50
	v_add_f32_e32 v51, 1.0, v51
	v_rcp_f32_e32 v51, v51
	s_mov_b64 s[30:31], 0
	v_mul_f32_e32 v46, v46, v50
	v_mul_f32_e32 v38, v46, v38
	v_mul_f32_e32 v46, v47, v51
	v_mul_f32_e32 v39, v46, v39
	v_mul_f32_e32 v46, 0xbfb8aa3b, v49
	v_exp_f32_e32 v46, v46
	v_mul_f32_e32 v47, 0xbfb8aa3b, v48
	v_exp_f32_e32 v47, v47
	v_med3_f32 v38, v38, s46, v222
	v_add_f32_e32 v46, 1.0, v46
	v_rcp_f32_e32 v46, v46
	v_add_f32_e32 v47, 1.0, v47
	v_rcp_f32_e32 v47, v47
	v_med3_f32 v39, v39, s46, v222
	v_mul_f32_e32 v46, v49, v46
	v_mul_f32_e32 v41, v46, v41
	v_mov_b32_e32 v46, 0
	v_mul_f32_e32 v47, v48, v47
	v_cvt_pk_fp8_f32 v46, v38, v39
	v_mul_f32_e32 v38, 0xbfb8aa3b, v34
	v_mul_f32_e32 v40, v47, v40
	v_exp_f32_e32 v47, v38
	v_med3_f32 v40, v40, s46, v222
	v_med3_f32 v41, v41, s46, v222
	v_cvt_pk_fp8_f32 v46, v40, v41 op_sel:[0,0,1]
	v_add_f32_e32 v40, 1.0, v47
	v_pk_mul_f32 v[38:39], v[44:45], v[78:79] op_sel_hi:[1,0]
	v_rcp_f32_e32 v44, v40
	v_mul_f32_e32 v40, 0xbfb8aa3b, v35
	v_exp_f32_e32 v45, v40
	v_pk_mul_f32 v[40:41], v[42:43], v[78:79] op_sel_hi:[1,0]
	v_mul_f32_e32 v34, v34, v44
	v_mul_f32_e32 v34, v34, v40
	v_add_f32_e32 v40, 1.0, v45
	v_mul_f32_e32 v42, 0xbfb8aa3b, v36
	v_rcp_f32_e32 v40, v40
	v_exp_f32_e32 v42, v42
	v_med3_f32 v34, v34, s46, v222
	s_and_b64 vcc, exec, s[28:29]
	v_mul_f32_e32 v35, v35, v40
	v_add_f32_e32 v40, 1.0, v42
	v_mul_f32_e32 v35, v35, v41
	v_rcp_f32_e32 v40, v40
	v_mul_f32_e32 v41, 0xbfb8aa3b, v37
	v_exp_f32_e32 v41, v41
	v_med3_f32 v35, v35, s46, v222
	v_mul_f32_e32 v36, v36, v40
	v_mul_f32_e32 v36, v36, v38
	v_add_f32_e32 v38, 1.0, v41
	v_rcp_f32_e32 v38, v38
	v_mov_b32_e32 v40, 0
	v_cvt_pk_fp8_f32 v40, v34, v35
	v_med3_f32 v36, v36, s46, v222
	v_mul_f32_e32 v34, v37, v38
	v_mul_f32_e32 v34, v34, v39
	v_med3_f32 v34, v34, s46, v222
	v_cvt_pk_fp8_f32 v40, v36, v34 op_sel:[0,0,1]
	v_add_u32_e32 v34, v66, v84
	ds_write_b32 v34, v46
	v_add_u32_e32 v34, v66, v74
	ds_write_b32 v34, v40
	s_cbranch_vccz .LBB0_721
	s_waitcnt lgkmcnt(0)
	s_barrier
	s_add_i32 s1, 0, 0x14000
	v_and_b32_e32 v225, 15, v223
	v_ashrrev_i32_e32 v224, 4, v223
	v_mov_b32_e32 v34, 0
	v_lshlrev_b32_e32 v194, 5, v223
	v_lshl_add_u32 v196, v225, 8, s1
	v_lshlrev_b32_e32 v197, 1, v224
	s_mov_b32 s1, 0
	s_mov_b32 s28, 64
	s_mov_b32 s29, 0
	v_mov_b32_e32 v35, v34
	v_mov_b32_e32 v36, v34
	v_mov_b32_e32 v37, v34
	v_mov_b32_e32 v38, v34
	v_mov_b32_e32 v39, v34
	v_mov_b32_e32 v40, v34
	v_mov_b32_e32 v41, v34
	v_mov_b32_e32 v42, v34
	v_mov_b32_e32 v43, v34
	v_mov_b32_e32 v44, v34
	v_mov_b32_e32 v45, v34
	v_mov_b32_e32 v46, v34
	v_mov_b32_e32 v47, v34
	v_mov_b32_e32 v48, v34
	v_mov_b32_e32 v49, v34
	v_mov_b32_e32 v50, v34
	v_mov_b32_e32 v51, v34
	v_mov_b32_e32 v52, v34
	v_mov_b32_e32 v53, v34
	v_mov_b32_e32 v54, v34
	v_mov_b32_e32 v55, v34
	v_mov_b32_e32 v56, v34
	v_mov_b32_e32 v57, v34
	v_mov_b32_e32 v58, v34
	v_mov_b32_e32 v59, v34
	v_mov_b32_e32 v60, v34
	v_mov_b32_e32 v61, v34
	v_mov_b32_e32 v62, v34
	v_mov_b32_e32 v63, v34
	v_mov_b32_e32 v64, v34
	v_mov_b32_e32 v65, v34
	v_mov_b32_e32 v66, v34
	v_mov_b32_e32 v67, v34
	v_mov_b32_e32 v68, v34
	v_mov_b32_e32 v69, v34
	v_mov_b32_e32 v70, v34
	v_mov_b32_e32 v71, v34
	v_mov_b32_e32 v72, v34
	v_mov_b32_e32 v73, v34
	v_mov_b32_e32 v74, v34
	v_mov_b32_e32 v75, v34
	v_mov_b32_e32 v76, v34
	v_mov_b32_e32 v77, v34
	v_mov_b32_e32 v78, v34
	v_mov_b32_e32 v79, v34
	v_mov_b32_e32 v80, v34
	v_mov_b32_e32 v81, v34
	v_mov_b32_e32 v82, v34
	v_mov_b32_e32 v83, v34
	v_mov_b32_e32 v84, v34
	v_mov_b32_e32 v85, v34
	v_mov_b32_e32 v86, v34
	v_mov_b32_e32 v87, v34
	v_mov_b32_e32 v88, v34
	v_mov_b32_e32 v89, v34
	v_mov_b32_e32 v90, v34
	v_mov_b32_e32 v91, v34
	v_mov_b32_e32 v92, v34
	v_mov_b32_e32 v93, v34
	v_mov_b32_e32 v94, v34
	v_mov_b32_e32 v95, v34
	v_mov_b32_e32 v96, v34
	v_mov_b32_e32 v97, v34
	v_mov_b32_e32 v98, v34
	v_mov_b32_e32 v99, v34
	v_mov_b32_e32 v100, v34
	v_mov_b32_e32 v101, v34
	v_mov_b32_e32 v102, v34
	v_mov_b32_e32 v103, v34
	v_mov_b32_e32 v104, v34
	v_mov_b32_e32 v105, v34
	v_mov_b32_e32 v106, v34
	v_mov_b32_e32 v107, v34
	v_mov_b32_e32 v108, v34
	v_mov_b32_e32 v109, v34
	v_mov_b32_e32 v110, v34
	v_mov_b32_e32 v111, v34
	v_mov_b32_e32 v112, v34
	v_mov_b32_e32 v113, v34
